# v5 + code placement: one 4-byte pad before the in-proj GEMM restores the baseline's byte phase (0 mod 8) of the GEMM main loops
# baseline (speedup 1.0000x reference)
;     __host__ __device__ bool next(int i, Unit& u) const {
;         const long L = (long)i * G + c; if (L >= nwg) return false;
;         int wgid = (int)L; { const int q = nwg / NXCD, r = nwg % NXCD, xcd = wgid % NXCD, off = wgid / NXCD; wgid = (xcd < r ? xcd * (q + 1) : r * (q + 1) + (xcd - r) * q) + off; }
;         const int nig = WGM * nN, gid = wgid / nig, fm = gid * WGM, gsz = (nM - fm) < WGM ? (nM - fm) : WGM;
;         u.pm = fm + ((wgid % nig) % gsz); u.pn = (wgid % nig) / gsz; return true;
; __global__ void __launch_bounds__(NWAVES * 64, 2) mk_fwd(Args args) {
;     ...
;         { pg8::Gemm g{(const pg8::bf16_t*)F.H1Q, F.WIN, M, NPROJ, D / 2}; pg8::StaticOrder S; S.init(M, NPROJ, F.G, (int)blockIdx.x);
;           pg8::EpiQ8 E{F.PROJ, NPROJ, 2048 / 256, F.SA, F.SW, 1};
;           pg8::gemm_phase<pg8::EpiQ8, pg8::StaticOrder, PG8_ALIGN, PG8_SP2, true>(F.lds, g, S, E); }
.LBB0_264:
	v_readlane_b32 s4, v252, 4
	s_cmp_lt_i32 s4, 3
	s_cselect_b64 s[2:3], -1, 0
	s_add_u32 s66, s48, 0x8000000
	s_addc_u32 s67, s49, 0
	s_add_u32 s60, s48, 0x14000000
	s_addc_u32 s61, s49, 0
	s_add_u32 s70, s48, 0x12000000
	s_addc_u32 s71, s49, 0
	v_readlane_b32 s6, v252, 6
	v_readlane_b32 s7, v252, 7
	s_add_u32 s64, s48, 0x3a0000
	s_addc_u32 s65, s49, 0
	s_and_b64 s[6:7], s[2:3], s[0:1]
	s_andn2_b64 vcc, exec, s[6:7]
	v_readlane_b32 s5, v252, 5
	s_cbranch_vccnz .LBB0_373
	s_nop 0
	s_cmpk_lt_i32 s58, 0x500
	s_cselect_b64 s[0:1], -1, 0
	s_cmpk_gt_i32 s58, 0x4ff
	v_readfirstlane_b32 s16, v0
	s_cbranch_scc1 .LBB0_267
	s_ashr_i32 s2, s58, 31
	s_lshr_b32 s2, s2, 29
	s_add_i32 s2, s58, s2
	s_ashr_i32 s3, s2, 3
	s_and_b32 s2, s2, -8
	s_sub_i32 s2, s58, s2
	s_cmp_lt_i32 s2, 0
	s_movk_i32 s4, 0xa1
	s_cselect_b32 s4, s4, 0xa0
	s_mul_i32 s2, s2, s4
	s_add_i32 s2, s2, s3
	s_mul_hi_i32 s3, s2, 0x66666667
	s_lshr_b32 s4, s3, 31
	s_ashr_i32 s3, s3, 6
	s_add_i32 s3, s3, s4
	s_lshl_b32 s4, s3, 3
	s_mulk_i32 s3, 0xa0
	s_sub_i32 s2, s2, s3
	s_sext_i32_i16 s3, s2
	s_bfe_u32 s3, s3, 0x3001c
	s_add_i32 s3, s2, s3
	s_sext_i32_i16 s5, s3
	s_and_b32 s3, s3, 0xfff8
	s_sub_i32 s2, s2, s3
	s_sext_i32_i16 s2, s2
	s_add_i32 s4, s4, s2
	s_ashr_i32 s2, s5, 3
